# scatter dst/src preloads moved to kernel entry; final_kernel kernarg loads issued together at entry
# baseline (speedup 1.0000x reference)
_Z14scatter_kernelPKiS0_S0_PiP15HIP_vector_typeIiLj2EE:
	s_load_dwordx4 s[52:55], s[0:1], 0x0
	s_mul_i32 s56, s2, 0x2710
	s_mov_b64 s[58:59], 0x1000
	s_mov_b64 s[60:61], 0x9000
	v_add_u32_e32 v120, s56, v0
	v_mov_b32_e32 v121, 0
	v_lshlrev_b64 v[120:121], 2, v[120:121]
	v_cmp_gt_u32_e32 vcc, 0x310, v0
	s_waitcnt lgkmcnt(0)
	v_lshl_add_u64 v[122:123], s[52:53], 0, v[120:121]
	v_lshl_add_u64 v[120:121], s[54:55], 0, v[120:121]
	v_lshl_add_u64 v[124:125], v[120:121], 0, s[60:61]
	v_lshl_add_u64 v[126:127], v[122:123], 0, s[60:61]
	s_and_saveexec_b64 s[62:63], vcc
	global_load_dword v109, v[124:125], off
	global_load_dword v119, v[126:127], off
	s_or_b64 exec, exec, s[62:63]
	global_load_dword v100, v[120:121], off
	v_lshl_add_u64 v[120:121], v[120:121], 0, s[58:59]
	global_load_dword v101, v[120:121], off
	v_lshl_add_u64 v[120:121], v[120:121], 0, s[58:59]
	global_load_dword v102, v[120:121], off
	v_lshl_add_u64 v[120:121], v[120:121], 0, s[58:59]
	global_load_dword v103, v[120:121], off
	v_lshl_add_u64 v[120:121], v[120:121], 0, s[58:59]
	global_load_dword v104, v[120:121], off
	v_lshl_add_u64 v[120:121], v[120:121], 0, s[58:59]
	global_load_dword v105, v[120:121], off
	v_lshl_add_u64 v[120:121], v[120:121], 0, s[58:59]
	global_load_dword v106, v[120:121], off
	v_lshl_add_u64 v[120:121], v[120:121], 0, s[58:59]
	global_load_dword v107, v[120:121], off
	v_lshl_add_u64 v[120:121], v[120:121], 0, s[58:59]
	global_load_dword v108, v[120:121], off
	global_load_dword v110, v[122:123], off
	v_lshl_add_u64 v[122:123], v[122:123], 0, s[58:59]
	global_load_dword v111, v[122:123], off
	v_lshl_add_u64 v[122:123], v[122:123], 0, s[58:59]
	global_load_dword v112, v[122:123], off
	v_lshl_add_u64 v[122:123], v[122:123], 0, s[58:59]
	global_load_dword v113, v[122:123], off
	v_lshl_add_u64 v[122:123], v[122:123], 0, s[58:59]
	global_load_dword v114, v[122:123], off
	v_lshl_add_u64 v[122:123], v[122:123], 0, s[58:59]
	global_load_dword v115, v[122:123], off
	v_lshl_add_u64 v[122:123], v[122:123], 0, s[58:59]
	global_load_dword v116, v[122:123], off
	v_lshl_add_u64 v[122:123], v[122:123], 0, s[58:59]
	global_load_dword v117, v[122:123], off
	v_lshl_add_u64 v[122:123], v[122:123], 0, s[58:59]
	global_load_dword v118, v[122:123], off
	s_load_dwordx4 s[12:15], s[0:1], 0x18
	s_movk_i32 s3, 0x31f
	v_cmp_lt_u32_e64 s[4:5], s3, v0
	s_movk_i32 s3, 0x320
	v_cmp_gt_u32_e32 vcc, s3, v0
	v_mov_b32_e32 v80, 0
	v_lshlrev_b32_e32 v2, 3, v0
	v_mov_b32_e32 v1, 0
	v_mov_b32_e32 v79, 0
	v_mov_b32_e32 v78, 0
	v_mov_b32_e32 v3, 0
	v_mov_b32_e32 v81, 0
	s_and_saveexec_b64 s[10:11], vcc
	s_cbranch_execz .LBB1_3
	s_load_dwordx2 s[6:7], s[0:1], 0x10
	v_mov_b32_e32 v3, 0
	s_mov_b64 s[8:9], 0x19000
	s_mov_b32 s3, 0
	s_mov_b32 s18, 0xfffeb000
	s_waitcnt lgkmcnt(0)
	v_lshl_add_u64 v[4:5], s[6:7], 0, v[2:3]
	v_lshl_add_u64 v[4:5], v[4:5], 0, s[8:9]
	s_mov_b32 s19, 0xfffec000
	s_mov_b32 s20, 0xfffee000
	s_mov_b32 s21, 0xfffef000
	s_mov_b32 s22, 0xffff1000
	s_mov_b32 s23, 0xffff2000
	s_mov_b32 s24, 0xffff4000
	s_mov_b32 s25, 0xffff6000
	s_mov_b32 s26, 0xffff7000
	s_movk_i32 s27, 0x9000
	s_movk_i32 s28, 0xa000
	s_movk_i32 s29, 0xc000
	s_movk_i32 s30, 0xd000
	s_movk_i32 s31, 0xf000
	s_movk_i32 s33, 0x1000
	s_movk_i32 s34, 0x3000
	s_movk_i32 s35, 0x4000
	s_movk_i32 s36, 0x6000
	s_movk_i32 s37, 0x7000
	s_mov_b32 s38, 0x9000
	s_mov_b32 s39, 0xa000
	s_mov_b32 s40, 0xc000
	s_mov_b32 s41, 0xe000
	s_mov_b32 s42, 0xf000
	s_mov_b32 s43, 0x11000
	s_mov_b32 s44, 0x12000
	s_mov_b32 s45, 0x14000
	s_mov_b32 s46, 0x15000
	s_mov_b32 s47, 0x17000
	s_mov_b64 s[16:17], 0x32000
	v_mov_b32_e32 v81, v3
	v_mov_b32_e32 v79, v3
	v_mov_b32_e32 v78, v3
	v_mov_b32_e32 v1, v3
	v_mov_b32_e32 v80, v3

.Lscat_loads:
	v_cmp_gt_u32_e32 vcc, 0x310, v0
	v_add_u32_e32 v13, s4, v0
	s_waitcnt vmcnt(0)
	v_ashrrev_i32_e32 v50, 6, v100
	v_lshl_add_u32 v60, v50, 2, v1
	ds_add_rtn_u32 v60, v60, v6
	v_lshlrev_b32_e32 v100, 20, v100
	v_mov_b32_e32 v70, v13
	v_and_or_b32 v100, v100, s5, v70
	v_ashrrev_i32_e32 v51, 6, v101
	v_lshl_add_u32 v61, v51, 2, v1
	ds_add_rtn_u32 v61, v61, v6
	v_lshlrev_b32_e32 v101, 20, v101
	v_add_u32_e32 v71, 0x400, v13
	v_and_or_b32 v101, v101, s5, v71
	v_ashrrev_i32_e32 v52, 6, v102
	v_lshl_add_u32 v62, v52, 2, v1
	ds_add_rtn_u32 v62, v62, v6
	v_lshlrev_b32_e32 v102, 20, v102
	v_add_u32_e32 v72, 0x800, v13
	v_and_or_b32 v102, v102, s5, v72
	v_ashrrev_i32_e32 v53, 6, v103
	v_lshl_add_u32 v63, v53, 2, v1
	ds_add_rtn_u32 v63, v63, v6
	v_lshlrev_b32_e32 v103, 20, v103
	v_add_u32_e32 v73, 0xc00, v13
	v_and_or_b32 v103, v103, s5, v73
	v_ashrrev_i32_e32 v54, 6, v104
	v_lshl_add_u32 v64, v54, 2, v1
	ds_add_rtn_u32 v64, v64, v6
	v_lshlrev_b32_e32 v104, 20, v104
	v_add_u32_e32 v74, 0x1000, v13
	v_and_or_b32 v104, v104, s5, v74
	v_ashrrev_i32_e32 v55, 6, v105
	v_lshl_add_u32 v65, v55, 2, v1
	ds_add_rtn_u32 v65, v65, v6
	v_lshlrev_b32_e32 v105, 20, v105
	v_add_u32_e32 v75, 0x1400, v13
	v_and_or_b32 v105, v105, s5, v75
	v_ashrrev_i32_e32 v56, 6, v106
	v_lshl_add_u32 v66, v56, 2, v1
	ds_add_rtn_u32 v66, v66, v6
	v_lshlrev_b32_e32 v106, 20, v106
	v_add_u32_e32 v76, 0x1800, v13
	v_and_or_b32 v106, v106, s5, v76
	v_ashrrev_i32_e32 v57, 6, v107
	v_lshl_add_u32 v67, v57, 2, v1
	ds_add_rtn_u32 v67, v67, v6
	v_lshlrev_b32_e32 v107, 20, v107
	v_add_u32_e32 v77, 0x1c00, v13
	v_and_or_b32 v107, v107, s5, v77
	v_ashrrev_i32_e32 v58, 6, v108
	v_lshl_add_u32 v68, v58, 2, v1
	ds_add_rtn_u32 v68, v68, v6
	v_lshlrev_b32_e32 v108, 20, v108
	v_add_u32_e32 v78, 0x2000, v13
	v_and_or_b32 v108, v108, s5, v78
	s_and_saveexec_b64 s[0:1], vcc
	v_ashrrev_i32_e32 v59, 6, v109
	v_lshl_add_u32 v69, v59, 2, v1
	ds_add_rtn_u32 v69, v69, v6
	v_lshlrev_b32_e32 v109, 20, v109
	v_add_u32_e32 v79, 0x2400, v13
	v_and_or_b32 v109, v109, s5, v79
	s_or_b64 exec, exec, s[0:1]
	s_waitcnt lgkmcnt(0)
	v_lshlrev_b32_e32 v70, 2, v60
	v_lshl_add_u32 v60, v60, 1, s6
	ds_write_b32 v70, v100
	ds_write_b16 v60, v50
	ds_write_b32 v70, v110 offset:40000
	v_lshlrev_b32_e32 v71, 2, v61
	v_lshl_add_u32 v61, v61, 1, s6
	ds_write_b32 v71, v101
	ds_write_b16 v61, v51
	ds_write_b32 v71, v111 offset:40000
	v_lshlrev_b32_e32 v72, 2, v62
	v_lshl_add_u32 v62, v62, 1, s6
	ds_write_b32 v72, v102
	ds_write_b16 v62, v52
	ds_write_b32 v72, v112 offset:40000
	v_lshlrev_b32_e32 v73, 2, v63
	v_lshl_add_u32 v63, v63, 1, s6
	ds_write_b32 v73, v103
	ds_write_b16 v63, v53
	ds_write_b32 v73, v113 offset:40000
	v_lshlrev_b32_e32 v74, 2, v64
	v_lshl_add_u32 v64, v64, 1, s6
	ds_write_b32 v74, v104
	ds_write_b16 v64, v54
	ds_write_b32 v74, v114 offset:40000
	v_lshlrev_b32_e32 v75, 2, v65
	v_lshl_add_u32 v65, v65, 1, s6
	ds_write_b32 v75, v105
	ds_write_b16 v65, v55
	ds_write_b32 v75, v115 offset:40000
	v_lshlrev_b32_e32 v76, 2, v66
	v_lshl_add_u32 v66, v66, 1, s6
	ds_write_b32 v76, v106
	ds_write_b16 v66, v56
	ds_write_b32 v76, v116 offset:40000
	v_lshlrev_b32_e32 v77, 2, v67
	v_lshl_add_u32 v67, v67, 1, s6
	ds_write_b32 v77, v107
	ds_write_b16 v67, v57
	ds_write_b32 v77, v117 offset:40000
	v_lshlrev_b32_e32 v78, 2, v68
	v_lshl_add_u32 v68, v68, 1, s6
	ds_write_b32 v78, v108
	ds_write_b16 v68, v58
	ds_write_b32 v78, v118 offset:40000
	s_and_saveexec_b64 s[0:1], vcc
	v_lshlrev_b32_e32 v79, 2, v69
	v_lshl_add_u32 v69, v69, 1, s6
	ds_write_b32 v79, v109
	ds_write_b16 v69, v59
	ds_write_b32 v79, v119 offset:40000
	s_or_b64 exec, exec, s[0:1]
	v_add_u32_e32 v1, 0x13880, v10
	v_lshlrev_b32_e32 v2, 2, v0
	s_mov_b64 s[0:1], 0
	s_movk_i32 s2, 0x230f
	s_waitcnt lgkmcnt(0)
	s_barrier

	.amdhsa_kernel _Z14scatter_kernelPKiS0_S0_PiP15HIP_vector_typeIiLj2EE
		.amdhsa_group_segment_fixed_size 124704
		.amdhsa_private_segment_fixed_size 0
		.amdhsa_kernarg_size 40
		.amdhsa_user_sgpr_count 2
		.amdhsa_user_sgpr_dispatch_ptr 0
		.amdhsa_user_sgpr_queue_ptr 0
		.amdhsa_user_sgpr_kernarg_segment_ptr 1
		.amdhsa_user_sgpr_dispatch_id 0
		.amdhsa_user_sgpr_kernarg_preload_length 0
		.amdhsa_user_sgpr_kernarg_preload_offset 0
		.amdhsa_user_sgpr_private_segment_size 0
		.amdhsa_uses_dynamic_stack 0
		.amdhsa_enable_private_segment 0
		.amdhsa_system_sgpr_workgroup_id_x 1
		.amdhsa_system_sgpr_workgroup_id_y 0
		.amdhsa_system_sgpr_workgroup_id_z 0
		.amdhsa_system_sgpr_workgroup_info 0
		.amdhsa_system_vgpr_workitem_id 0
		.amdhsa_next_free_vgpr 128
		.amdhsa_next_free_sgpr 96
		.amdhsa_accum_offset 128
		.amdhsa_reserve_vcc 1
		.amdhsa_float_round_mode_32 0
		.amdhsa_float_round_mode_16_64 0
		.amdhsa_float_denorm_mode_32 3
		.amdhsa_float_denorm_mode_16_64 3
		.amdhsa_dx10_clamp 1
		.amdhsa_ieee_mode 1
		.amdhsa_fp16_overflow 0
		.amdhsa_tg_split 0
		.amdhsa_exception_fp_ieee_invalid_op 0
		.amdhsa_exception_fp_denorm_src 0
		.amdhsa_exception_fp_ieee_div_zero 0
		.amdhsa_exception_fp_ieee_overflow 0
		.amdhsa_exception_fp_ieee_underflow 0
		.amdhsa_exception_fp_ieee_inexact 0
		.amdhsa_exception_int_div_zero 0
	.end_amdhsa_kernel

_Z12final_kernelPKDv8_DF16_S1_PKfS3_S3_S1_S3_Pf:
	s_load_dword s3, s[0:1], 0x40
	s_load_dwordx4 s[8:11], s[0:1], 0x0
	s_load_dwordx4 s[24:27], s[0:1], 0x28
	s_waitcnt lgkmcnt(0)
	s_ashr_i32 s4, s3, 3
	s_and_b32 s5, s3, 7
	s_and_b32 s3, s2, 7
	s_add_i32 s14, s4, 1
	s_cmp_ge_u32 s3, s5
	s_cbranch_scc0 .LBB3_2
	s_mul_i32 s6, s14, s5
	s_sub_i32 s5, s3, s5
	s_mul_i32 s5, s5, s4
	s_add_i32 s15, s6, s5
	s_cbranch_execz .LBB3_3
	s_branch .LBB3_4
.LBB3_2:
.LBB3_3:
	s_mul_i32 s15, s14, s3
.LBB3_4:
	s_mov_b64 s[4:5], s[24:25]
	s_mov_b64 s[6:7], s[26:27]
	s_lshr_b32 s2, s2, 3
	s_add_i32 s2, s15, s2
	s_lshl_b32 s18, s2, 6
	v_lshrrev_b32_e32 v20, 4, v0
	v_or_b32_e32 v6, s18, v20
	v_min_i32_e32 v2, 0x1869f, v6
	v_and_b32_e32 v1, 15, v0
	v_ashrrev_i32_e32 v3, 31, v2
	v_lshlrev_b64 v[2:3], 8, v[2:3]
	v_lshlrev_b32_e32 v8, 4, v1
	v_or_b32_e32 v2, v2, v8
	s_waitcnt lgkmcnt(0)
	v_lshl_add_u64 v[4:5], s[8:9], 0, v[2:3]
	v_lshl_add_u64 v[2:3], s[10:11], 0, v[2:3]
	global_load_dwordx4 v[14:17], v[2:3], off nt
	v_or_b32_e32 v2, 32, v6
	v_min_i32_e32 v2, 0x1869f, v2
	v_ashrrev_i32_e32 v3, 31, v2
	v_lshlrev_b64 v[6:7], 8, v[2:3]
	v_or_b32_e32 v6, v6, v8
	v_lshl_add_u64 v[2:3], s[8:9], 0, v[6:7]
	v_lshl_add_u64 v[6:7], s[10:11], 0, v[6:7]
	global_load_dwordx4 v[10:13], v[4:5], off
	s_load_dwordx2 s[2:3], s[0:1], 0x38
	global_load_dwordx4 v[2:5], v[2:3], off
	s_movk_i32 s8, 0x80
	global_load_dwordx4 v[6:9], v[6:7], off nt
	v_cmp_gt_u32_e32 vcc, s8, v0
	v_mov_b32_e32 v19, 0
	s_and_saveexec_b64 s[12:13], vcc
	s_cbranch_execz .LBB3_6
	s_load_dwordx4 s[8:11], s[0:1], 0x10
	s_load_dwordx2 s[14:15], s[0:1], 0x20
	v_lshlrev_b32_e32 v18, 2, v0
	s_mov_b32 s16, 0
	s_mov_b32 s17, 0x40f86a00
	s_waitcnt lgkmcnt(0)
	global_load_dword v25, v18, s[8:9]
	global_load_dword v24, v18, s[8:9] offset:512
	global_load_dword v27, v18, s[8:9] offset:1024
	global_load_dword v26, v18, s[8:9] offset:1536
	global_load_dword v29, v18, s[8:9] offset:2048
	global_load_dword v28, v18, s[8:9] offset:2560
	global_load_dword v31, v18, s[8:9] offset:3072
	global_load_dword v30, v18, s[8:9] offset:3584
	v_lshl_add_u64 v[22:23], s[8:9], 0, v[18:19]
	v_add_co_u32_e32 v22, vcc, 0x1000, v22
	s_brev_b32 s8, 1
	s_nop 0
	v_addc_co_u32_e32 v23, vcc, 0, v23, vcc
	global_load_dword v33, v[22:23], off
	global_load_dword v32, v[22:23], off offset:512
	global_load_dword v35, v[22:23], off offset:1024
	global_load_dword v34, v[22:23], off offset:1536
	global_load_dword v37, v[22:23], off offset:2048
	global_load_dword v36, v[22:23], off offset:2560
	global_load_dword v39, v[22:23], off offset:3072
	global_load_dword v38, v[22:23], off offset:3584
	v_lshrrev_b32_e32 v23, 1, v0
	v_and_b32_e32 v22, 7, v0
	v_and_b32_e32 v23, 60, v23
	v_or_b32_e32 v40, v23, v22
	v_add3_u32 v23, v22, v23, 60
	v_cmp_gt_u32_e32 vcc, 4, v22
	s_mov_b32 s9, 0x3ee4f8b5
	s_mov_b32 s20, 0
	v_cndmask_b32_e32 v22, v23, v40, vcc
	v_lshlrev_b32_e32 v22, 2, v22
	global_load_dword v42, v22, s[10:11]
	global_load_dword v43, v22, s[14:15]
	s_brev_b32 s21, 8
	v_mov_b32_e32 v21, 0x100
	s_waitcnt vmcnt(16)
	v_pk_add_f32 v[22:23], v[24:25], 0 op_sel_hi:[1,0]
	s_waitcnt vmcnt(14)
	v_pk_add_f32 v[22:23], v[22:23], v[26:27]
	s_waitcnt vmcnt(12)
	v_pk_add_f32 v[22:23], v[22:23], v[28:29]
	s_waitcnt vmcnt(10)
	v_pk_add_f32 v[22:23], v[22:23], v[30:31]
	s_waitcnt vmcnt(8)
	v_pk_add_f32 v[22:23], v[22:23], v[32:33]
	s_waitcnt vmcnt(6)
	v_pk_add_f32 v[22:23], v[22:23], v[34:35]
	s_waitcnt vmcnt(4)
	v_pk_add_f32 v[22:23], v[22:23], v[36:37]
	s_waitcnt vmcnt(2)
	v_pk_add_f32 v[22:23], v[22:23], v[38:39]
	s_nop 0
	v_cvt_f64_f32_e32 v[24:25], v23
	v_cvt_f64_f32_e32 v[22:23], v22
	v_div_scale_f64 v[26:27], s[0:1], s[16:17], s[16:17], v[22:23]
	v_div_scale_f64 v[30:31], s[0:1], s[16:17], s[16:17], v[24:25]
	v_rcp_f64_e32 v[32:33], v[26:27]
	v_rcp_f64_e32 v[34:35], v[30:31]
	v_div_scale_f64 v[28:29], vcc, v[22:23], s[16:17], v[22:23]
	v_fma_f64 v[38:39], -v[26:27], v[32:33], 1.0
	v_fma_f64 v[40:41], -v[30:31], v[34:35], 1.0
	v_fmac_f64_e32 v[32:33], v[32:33], v[38:39]
	v_fmac_f64_e32 v[34:35], v[34:35], v[40:41]
	v_fma_f64 v[38:39], -v[26:27], v[32:33], 1.0
	v_fma_f64 v[40:41], -v[30:31], v[34:35], 1.0
	v_fmac_f64_e32 v[32:33], v[32:33], v[38:39]
	v_div_scale_f64 v[36:37], s[0:1], v[24:25], s[16:17], v[24:25]
	v_fmac_f64_e32 v[34:35], v[34:35], v[40:41]
	v_mul_f64 v[38:39], v[28:29], v[32:33]
	v_mul_f64 v[40:41], v[36:37], v[34:35]
	v_fma_f64 v[26:27], -v[26:27], v[38:39], v[28:29]
	v_fma_f64 v[28:29], -v[30:31], v[40:41], v[36:37]
	v_div_fmas_f64 v[26:27], v[26:27], v[32:33], v[38:39]
	s_mov_b64 vcc, s[0:1]
	v_div_fixup_f64 v[22:23], v[26:27], s[16:17], v[22:23]
	v_div_fmas_f64 v[26:27], v[28:29], v[34:35], v[40:41]
	v_div_fixup_f64 v[24:25], v[26:27], s[16:17], v[24:25]
	v_fma_f64 v[22:23], -v[24:25], v[24:25], v[22:23]
	v_cmp_ngt_f64_e32 vcc, 0, v[22:23]
	v_mov_b32_e32 v32, 0x260
	s_nop 0
	v_cndmask_b32_e32 v23, 0, v23, vcc
	v_cndmask_b32_e32 v22, 0, v22, vcc
	v_add_f64 v[22:23], v[22:23], s[8:9]
	v_cmp_gt_f64_e32 vcc, s[20:21], v[22:23]
	s_nop 1
	v_cndmask_b32_e32 v21, 0, v21, vcc
	v_ldexp_f64 v[22:23], v[22:23], v21
	v_rsq_f64_e32 v[26:27], v[22:23]
	v_mov_b32_e32 v21, 0xffffff80
	v_cndmask_b32_e32 v21, 0, v21, vcc
	v_cmp_class_f64_e32 vcc, v[22:23], v32
	v_mul_f64 v[28:29], v[22:23], v[26:27]
	v_mul_f64 v[26:27], v[26:27], 0.5
	v_fma_f64 v[30:31], -v[26:27], v[28:29], 0.5
	v_fmac_f64_e32 v[28:29], v[28:29], v[30:31]
	v_fmac_f64_e32 v[26:27], v[26:27], v[30:31]
	v_fma_f64 v[30:31], -v[28:29], v[28:29], v[22:23]
	v_fmac_f64_e32 v[28:29], v[30:31], v[26:27]
	v_fma_f64 v[30:31], -v[28:29], v[28:29], v[22:23]
	v_fmac_f64_e32 v[28:29], v[30:31], v[26:27]
	v_ldexp_f64 v[26:27], v[28:29], v21
	v_cndmask_b32_e32 v23, v27, v23, vcc
	v_cndmask_b32_e32 v22, v26, v22, vcc
	v_div_scale_f64 v[26:27], s[0:1], v[22:23], v[22:23], 1.0
	v_rcp_f64_e32 v[28:29], v[26:27]
	v_div_scale_f64 v[30:31], vcc, 1.0, v[22:23], 1.0
	v_fma_f64 v[32:33], -v[26:27], v[28:29], 1.0
	v_fmac_f64_e32 v[28:29], v[28:29], v[32:33]
	v_fma_f64 v[32:33], -v[26:27], v[28:29], 1.0
	v_fmac_f64_e32 v[28:29], v[28:29], v[32:33]
	v_mul_f64 v[32:33], v[30:31], v[28:29]
	v_fma_f64 v[26:27], -v[26:27], v[32:33], v[30:31]
	v_div_fmas_f64 v[26:27], v[26:27], v[28:29], v[32:33]
	v_div_fixup_f64 v[22:23], v[26:27], v[22:23], 1.0
	v_cvt_f32_f64_e32 v21, v[22:23]
	s_waitcnt vmcnt(1)
	v_mul_f32_e32 v21, v42, v21
	v_cvt_f32_f64_e32 v22, v[24:25]
	s_waitcnt vmcnt(0)
	v_fma_f32 v22, -v21, v22, v43
	ds_write2st64_b32 v18, v21, v22 offset0:132 offset1:134

	.amdhsa_kernel _Z12final_kernelPKDv8_DF16_S1_PKfS3_S3_S1_S3_Pf
		.amdhsa_group_segment_fixed_size 34816
		.amdhsa_private_segment_fixed_size 0
		.amdhsa_kernarg_size 320
		.amdhsa_user_sgpr_count 2
		.amdhsa_user_sgpr_dispatch_ptr 0
		.amdhsa_user_sgpr_queue_ptr 0
		.amdhsa_user_sgpr_kernarg_segment_ptr 1
		.amdhsa_user_sgpr_dispatch_id 0
		.amdhsa_user_sgpr_kernarg_preload_length 0
		.amdhsa_user_sgpr_kernarg_preload_offset 0
		.amdhsa_user_sgpr_private_segment_size 0
		.amdhsa_uses_dynamic_stack 0
		.amdhsa_enable_private_segment 0
		.amdhsa_system_sgpr_workgroup_id_x 1
		.amdhsa_system_sgpr_workgroup_id_y 0
		.amdhsa_system_sgpr_workgroup_id_z 0
		.amdhsa_system_sgpr_workgroup_info 0
		.amdhsa_system_vgpr_workitem_id 0
		.amdhsa_next_free_vgpr 60
		.amdhsa_next_free_sgpr 28
		.amdhsa_accum_offset 60
		.amdhsa_reserve_vcc 1
		.amdhsa_float_round_mode_32 0
		.amdhsa_float_round_mode_16_64 0
		.amdhsa_float_denorm_mode_32 3
		.amdhsa_float_denorm_mode_16_64 3
		.amdhsa_dx10_clamp 1
		.amdhsa_ieee_mode 1
		.amdhsa_fp16_overflow 0
		.amdhsa_tg_split 0
		.amdhsa_exception_fp_ieee_invalid_op 0
		.amdhsa_exception_fp_denorm_src 0
		.amdhsa_exception_fp_ieee_div_zero 0
		.amdhsa_exception_fp_ieee_overflow 0
		.amdhsa_exception_fp_ieee_underflow 0
		.amdhsa_exception_fp_ieee_inexact 0
		.amdhsa_exception_int_div_zero 0
	.end_amdhsa_kernel

amdhsa.kernels:
  - .agpr_count:     0
    .args:
      - .actual_access:  read_only
        .address_space:  global
        .offset:         0
        .size:           8
        .value_kind:     global_buffer
      - .address_space:  global
        .offset:         8
        .size:           8
        .value_kind:     global_buffer
      - .actual_access:  read_only
        .address_space:  global
        .offset:         16
        .size:           8
        .value_kind:     global_buffer
      - .actual_access:  read_only
        .address_space:  global
        .offset:         24
        .size:           8
        .value_kind:     global_buffer
      - .actual_access:  write_only
        .address_space:  global
        .offset:         32
        .size:           8
        .value_kind:     global_buffer
      - .actual_access:  read_only
        .address_space:  global
        .offset:         40
        .size:           8
        .value_kind:     global_buffer
      - .actual_access:  write_only
        .address_space:  global
        .offset:         48
        .size:           8
        .value_kind:     global_buffer
      - .actual_access:  write_only
        .address_space:  global
        .offset:         56
        .size:           8
        .value_kind:     global_buffer
    .group_segment_fixed_size: 6400
    .kernarg_segment_align: 8
    .kernarg_segment_size: 64
    .language:       OpenCL C
    .language_version:
      - 2
      - 0
    .max_flat_workgroup_size: 1024
    .name:           _Z17prep_count_kernelPKfPDv8_DF16_S0_S0_S2_PKiPiP15HIP_vector_typeIfLj4EE
    .private_segment_fixed_size: 0
    .sgpr_count:     22
    .sgpr_spill_count: 0
    .symbol:         _Z17prep_count_kernelPKfPDv8_DF16_S0_S0_S2_PKiPiP15HIP_vector_typeIfLj4EE.kd
    .uniform_work_group_size: 1
    .uses_dynamic_stack: false
    .vgpr_count:     22
    .vgpr_spill_count: 0
    .wavefront_size: 64
  - .agpr_count:     0
    .args:
      - .actual_access:  read_only
        .address_space:  global
        .offset:         0
        .size:           8
        .value_kind:     global_buffer
      - .actual_access:  read_only
        .address_space:  global
        .offset:         8
        .size:           8
        .value_kind:     global_buffer
      - .actual_access:  read_only
        .address_space:  global
        .offset:         16
        .size:           8
        .value_kind:     global_buffer
      - .actual_access:  write_only
        .address_space:  global
        .offset:         24
        .size:           8
        .value_kind:     global_buffer
      - .actual_access:  write_only
        .address_space:  global
        .offset:         32
        .size:           8
        .value_kind:     global_buffer
    .group_segment_fixed_size: 124704
    .kernarg_segment_align: 8
    .kernarg_segment_size: 40
    .language:       OpenCL C
    .language_version:
      - 2
      - 0
    .max_flat_workgroup_size: 1024
    .name:           _Z14scatter_kernelPKiS0_S0_PiP15HIP_vector_typeIiLj2EE
    .private_segment_fixed_size: 0
    .sgpr_count:     55
    .sgpr_spill_count: 0
    .symbol:         _Z14scatter_kernelPKiS0_S0_PiP15HIP_vector_typeIiLj2EE.kd
    .uniform_work_group_size: 1
    .uses_dynamic_stack: false
    .vgpr_count:     128
    .vgpr_spill_count: 0
    .wavefront_size: 64
  - .agpr_count:     0
    .args:
      - .actual_access:  read_only
        .address_space:  global
        .offset:         0
        .size:           8
        .value_kind:     global_buffer
      - .address_space:  global
        .offset:         8
        .size:           8
        .value_kind:     global_buffer
      - .address_space:  global
        .offset:         16
        .size:           8
        .value_kind:     global_buffer
      - .actual_access:  read_only
        .address_space:  global
        .offset:         24
        .size:           8
        .value_kind:     global_buffer
      - .actual_access:  read_only
        .address_space:  global
        .offset:         32
        .size:           8
        .value_kind:     global_buffer
      - .actual_access:  read_only
        .address_space:  global
        .offset:         40
        .size:           8
        .value_kind:     global_buffer
      - .offset:         48
        .size:           4
        .value_kind:     hidden_block_count_x
      - .offset:         52
        .size:           4
        .value_kind:     hidden_block_count_y
      - .offset:         56
        .size:           4
        .value_kind:     hidden_block_count_z
      - .offset:         60
        .size:           2
        .value_kind:     hidden_group_size_x
      - .offset:         62
        .size:           2
        .value_kind:     hidden_group_size_y
      - .offset:         64
        .size:           2
        .value_kind:     hidden_group_size_z
      - .offset:         66
        .size:           2
        .value_kind:     hidden_remainder_x
      - .offset:         68
        .size:           2
        .value_kind:     hidden_remainder_y
      - .offset:         70
        .size:           2
        .value_kind:     hidden_remainder_z
      - .offset:         88
        .size:           8
        .value_kind:     hidden_global_offset_x
      - .offset:         96
        .size:           8
        .value_kind:     hidden_global_offset_y
      - .offset:         104
        .size:           8
        .value_kind:     hidden_global_offset_z
      - .offset:         112
        .size:           2
        .value_kind:     hidden_grid_dims
    .group_segment_fixed_size: 1024
    .kernarg_segment_align: 8
    .kernarg_segment_size: 304
    .language:       OpenCL C
    .language_version:
      - 2
      - 0
    .max_flat_workgroup_size: 256
    .name:           _Z9bn_kernelPKDv8_DF16_S1_PS_PKfS4_S4_
    .private_segment_fixed_size: 0
    .sgpr_count:     20
    .sgpr_spill_count: 0
    .symbol:         _Z9bn_kernelPKDv8_DF16_S1_PS_PKfS4_S4_.kd
    .uniform_work_group_size: 1
    .uses_dynamic_stack: false
    .vgpr_count:     64
    .vgpr_spill_count: 0
    .wavefront_size: 64
  - .agpr_count:     0
    .args:
      - .actual_access:  read_only
        .address_space:  global
        .offset:         0
        .size:           8
        .value_kind:     global_buffer
      - .actual_access:  read_only
        .address_space:  global
        .offset:         8
        .size:           8
        .value_kind:     global_buffer
      - .actual_access:  read_only
        .address_space:  global
        .offset:         16
        .size:           8
        .value_kind:     global_buffer
      - .actual_access:  read_only
        .address_space:  global
        .offset:         24
        .size:           8
        .value_kind:     global_buffer
      - .actual_access:  read_only
        .address_space:  global
        .offset:         32
        .size:           8
        .value_kind:     global_buffer
      - .actual_access:  read_only
        .address_space:  global
        .offset:         40
        .size:           8
        .value_kind:     global_buffer
      - .actual_access:  read_only
        .address_space:  global
        .offset:         48
        .size:           8
        .value_kind:     global_buffer
      - .actual_access:  write_only
        .address_space:  global
        .offset:         56
        .size:           8
        .value_kind:     global_buffer
      - .offset:         64
        .size:           4
        .value_kind:     hidden_block_count_x
      - .offset:         68
        .size:           4
        .value_kind:     hidden_block_count_y
      - .offset:         72
        .size:           4
        .value_kind:     hidden_block_count_z
      - .offset:         76
        .size:           2
        .value_kind:     hidden_group_size_x
      - .offset:         78
        .size:           2
        .value_kind:     hidden_group_size_y
      - .offset:         80
        .size:           2
        .value_kind:     hidden_group_size_z
      - .offset:         82
        .size:           2
        .value_kind:     hidden_remainder_x
      - .offset:         84
        .size:           2
        .value_kind:     hidden_remainder_y
      - .offset:         86
        .size:           2
        .value_kind:     hidden_remainder_z
      - .offset:         104
        .size:           8
        .value_kind:     hidden_global_offset_x
      - .offset:         112
        .size:           8
        .value_kind:     hidden_global_offset_y
      - .offset:         120
        .size:           8
        .value_kind:     hidden_global_offset_z
      - .offset:         128
        .size:           2
        .value_kind:     hidden_grid_dims
    .group_segment_fixed_size: 34816
    .kernarg_segment_align: 8
    .kernarg_segment_size: 320
    .language:       OpenCL C
    .language_version:
      - 2
      - 0
    .max_flat_workgroup_size: 512
    .name:           _Z12final_kernelPKDv8_DF16_S1_PKfS3_S3_S1_S3_Pf
    .private_segment_fixed_size: 0
    .sgpr_count:     34
    .sgpr_spill_count: 0
    .symbol:         _Z12final_kernelPKDv8_DF16_S1_PKfS3_S3_S1_S3_Pf.kd
    .uniform_work_group_size: 1
    .uses_dynamic_stack: false
    .vgpr_count:     60
    .vgpr_spill_count: 0
    .wavefront_size: 64
  - .agpr_count:     0
    .args:
      - .actual_access:  read_only
        .address_space:  global
        .offset:         0
        .size:           8
        .value_kind:     global_buffer
      - .actual_access:  read_only
        .address_space:  global
        .offset:         8
        .size:           8
        .value_kind:     global_buffer
      - .address_space:  global
        .offset:         16
        .size:           8
        .value_kind:     global_buffer
      - .actual_access:  write_only
        .address_space:  global
        .offset:         24
        .size:           8
        .value_kind:     global_buffer
      - .address_space:  global
        .offset:         32
        .size:           8
        .value_kind:     global_buffer
      - .address_space:  global
        .offset:         40
        .size:           8
        .value_kind:     global_buffer
      - .actual_access:  read_only
        .address_space:  global
        .offset:         48
        .size:           8
        .value_kind:     global_buffer
      - .actual_access:  read_only
        .address_space:  global
        .offset:         56
        .size:           8
        .value_kind:     global_buffer
      - .address_space:  global
        .offset:         64
        .size:           8
        .value_kind:     global_buffer
      - .address_space:  global
        .offset:         72
        .size:           8
        .value_kind:     global_buffer
      - .actual_access:  read_only
        .address_space:  global
        .offset:         80
        .size:           8
        .value_kind:     global_buffer
      - .actual_access:  read_only
        .address_space:  global
        .offset:         88
        .size:           8
        .value_kind:     global_buffer
      - .offset:         96
        .size:           4
        .value_kind:     hidden_block_count_x
      - .offset:         100
        .size:           4
        .value_kind:     hidden_block_count_y
      - .offset:         104
        .size:           4
        .value_kind:     hidden_block_count_z
      - .offset:         108
        .size:           2
        .value_kind:     hidden_group_size_x
      - .offset:         110
        .size:           2
        .value_kind:     hidden_group_size_y
      - .offset:         112
        .size:           2
        .value_kind:     hidden_group_size_z
      - .offset:         114
        .size:           2
        .value_kind:     hidden_remainder_x
      - .offset:         116
        .size:           2
        .value_kind:     hidden_remainder_y
      - .offset:         118
        .size:           2
        .value_kind:     hidden_remainder_z
      - .offset:         136
        .size:           8
        .value_kind:     hidden_global_offset_x
      - .offset:         144
        .size:           8
        .value_kind:     hidden_global_offset_y
      - .offset:         152
        .size:           8
        .value_kind:     hidden_global_offset_z
      - .offset:         160
        .size:           2
        .value_kind:     hidden_grid_dims
    .group_segment_fixed_size: 26384
    .kernarg_segment_align: 8
    .kernarg_segment_size: 352
    .language:       OpenCL C
    .language_version:
      - 2
      - 0
    .max_flat_workgroup_size: 512
    .name:           _Z12layer_kernelILb1ELi512ELi64EEvPKDv8_DF16_PKfPS0_PiS6_S6_S2_S4_S5_PfPK15HIP_vector_typeIiLj2EEPKi
    .private_segment_fixed_size: 0
    .sgpr_count:     52
    .sgpr_spill_count: 0
    .symbol:         _Z12layer_kernelILb1ELi512ELi64EEvPKDv8_DF16_PKfPS0_PiS6_S6_S2_S4_S5_PfPK15HIP_vector_typeIiLj2EEPKi.kd
    .uniform_work_group_size: 1
    .uses_dynamic_stack: false
    .vgpr_count:     61
    .vgpr_spill_count: 0
    .wavefront_size: 64
  - .agpr_count:     0
    .args:
      - .actual_access:  read_only
        .address_space:  global
        .offset:         0
        .size:           8
        .value_kind:     global_buffer
      - .actual_access:  read_only
        .address_space:  global
        .offset:         8
        .size:           8
        .value_kind:     global_buffer
      - .actual_access:  read_only
        .address_space:  global
        .offset:         16
        .size:           8
        .value_kind:     global_buffer
      - .actual_access:  read_only
        .address_space:  global
        .offset:         24
        .size:           8
        .value_kind:     global_buffer
      - .actual_access:  read_only
        .address_space:  global
        .offset:         32
        .size:           8
        .value_kind:     global_buffer
      - .actual_access:  read_only
        .address_space:  global
        .offset:         40
        .size:           8
        .value_kind:     global_buffer
      - .actual_access:  read_only
        .address_space:  global
        .offset:         48
        .size:           8
        .value_kind:     global_buffer
      - .actual_access:  read_only
        .address_space:  global
        .offset:         56
        .size:           8
        .value_kind:     global_buffer
      - .address_space:  global
        .offset:         64
        .size:           8
        .value_kind:     global_buffer
      - .address_space:  global
        .offset:         72
        .size:           8
        .value_kind:     global_buffer
      - .actual_access:  read_only
        .address_space:  global
        .offset:         80
        .size:           8
        .value_kind:     global_buffer
      - .actual_access:  read_only
        .address_space:  global
        .offset:         88
        .size:           8
        .value_kind:     global_buffer
      - .offset:         96
        .size:           4
        .value_kind:     hidden_block_count_x
      - .offset:         100
        .size:           4
        .value_kind:     hidden_block_count_y
      - .offset:         104
        .size:           4
        .value_kind:     hidden_block_count_z
      - .offset:         108
        .size:           2
        .value_kind:     hidden_group_size_x
      - .offset:         110
        .size:           2
        .value_kind:     hidden_group_size_y
      - .offset:         112
        .size:           2
        .value_kind:     hidden_group_size_z
      - .offset:         114
        .size:           2
        .value_kind:     hidden_remainder_x
      - .offset:         116
        .size:           2
        .value_kind:     hidden_remainder_y
      - .offset:         118
        .size:           2
        .value_kind:     hidden_remainder_z
      - .offset:         136
        .size:           8
        .value_kind:     hidden_global_offset_x
      - .offset:         144
        .size:           8
        .value_kind:     hidden_global_offset_y
      - .offset:         152
        .size:           8
        .value_kind:     hidden_global_offset_z
      - .offset:         160
        .size:           2
        .value_kind:     hidden_grid_dims
    .group_segment_fixed_size: 12932
    .kernarg_segment_align: 8
    .kernarg_segment_size: 352
    .language:       OpenCL C
    .language_version:
      - 2
      - 0
    .max_flat_workgroup_size: 256
    .name:           _Z12layer_kernelILb0ELi256ELi32EEvPKDv8_DF16_PKfPS0_PiS6_S6_S2_S4_S5_PfPK15HIP_vector_typeIiLj2EEPKi
    .private_segment_fixed_size: 0
    .sgpr_count:     36
    .sgpr_spill_count: 0
    .symbol:         _Z12layer_kernelILb0ELi256ELi32EEvPKDv8_DF16_PKfPS0_PiS6_S6_S2_S4_S5_PfPK15HIP_vector_typeIiLj2EEPKi.kd
    .uniform_work_group_size: 1
    .uses_dynamic_stack: false
    .vgpr_count:     64
    .vgpr_spill_count: 0
    .wavefront_size: 64
